# own-tile h1 stores deferred into the first own k-step as well
# baseline (speedup 1.0000x reference)
.LBB1_4:
	s_and_saveexec_b64 s[8:9], s[2:3]
	v_perm_b32 v5, v1, v102, s23
	v_perm_b32 v9, v121, v103, s23
	v_perm_b32 v17, v144, v115, s23
	v_perm_b32 v29, v145, v116, s23
	s_or_b64 exec, exec, s[8:9]
	v_mfma_f32_16x16x32_f16 v[164:167], v[30:33], v[2:5], 0
	v_mfma_f32_16x16x32_f16 v[180:183], v[22:25], v[2:5], 0
	s_cmp_lg_u32 s22, 0x818000
	v_mfma_f32_16x16x32_f16 v[168:171], v[30:33], v[6:9], 0
	v_mfma_f32_16x16x32_f16 v[184:187], v[22:25], v[6:9], 0
	s_cselect_b32 s9, s11, 15
	v_mfma_f32_16x16x32_f16 v[172:175], v[30:33], v[14:17], 0
	v_mfma_f32_16x16x32_f16 v[188:191], v[22:25], v[14:17], 0
	v_mfma_f32_16x16x32_f16 v[176:179], v[30:33], v[26:29], 0
	v_mfma_f32_16x16x32_f16 v[192:195], v[22:25], v[26:29], 0
	v_mfma_f32_16x16x32_f16 v[208:211], v[18:21], v[2:5], 0
	v_mfma_f32_16x16x32_f16 v[224:227], v[10:13], v[2:5], 0
	v_cvt_pk_f16_f32 v122, v164, v165
	v_cvt_pk_f16_f32 v123, v166, v167
	v_pk_max_f16 v122, v122, 0
	v_pk_max_f16 v123, v123, 0
	v_cvt_pk_f16_f32 v124, v180, v181
	v_cvt_pk_f16_f32 v125, v182, v183
	v_pk_max_f16 v124, v124, 0
	v_pk_max_f16 v125, v125, 0
	v_mfma_f32_16x16x32_f16 v[212:215], v[18:21], v[6:9], 0
	v_mfma_f32_16x16x32_f16 v[228:231], v[10:13], v[6:9], 0
	v_cvt_pk_f16_f32 v126, v168, v169
	v_cvt_pk_f16_f32 v127, v170, v171
	v_pk_max_f16 v126, v126, 0
	v_pk_max_f16 v127, v127, 0
	v_cvt_pk_f16_f32 v128, v184, v185
	v_cvt_pk_f16_f32 v129, v186, v187
	v_pk_max_f16 v128, v128, 0
	v_pk_max_f16 v129, v129, 0
	v_mfma_f32_16x16x32_f16 v[216:219], v[18:21], v[14:17], 0
	v_mfma_f32_16x16x32_f16 v[232:235], v[10:13], v[14:17], 0
	v_cvt_pk_f16_f32 v134, v172, v173
	v_cvt_pk_f16_f32 v135, v174, v175
	v_pk_max_f16 v134, v134, 0
	v_pk_max_f16 v135, v135, 0
	v_cvt_pk_f16_f32 v136, v188, v189
	v_cvt_pk_f16_f32 v137, v190, v191
	v_pk_max_f16 v136, v136, 0
	v_pk_max_f16 v137, v137, 0
	v_mfma_f32_16x16x32_f16 v[220:223], v[18:21], v[26:29], 0
	v_mfma_f32_16x16x32_f16 v[236:239], v[10:13], v[26:29], 0
	v_cvt_pk_f16_f32 v138, v176, v177
	v_cvt_pk_f16_f32 v139, v178, v179
	v_pk_max_f16 v138, v138, 0
	v_pk_max_f16 v139, v139, 0
	v_cvt_pk_f16_f32 v140, v192, v193
	v_cvt_pk_f16_f32 v141, v194, v195
	v_pk_max_f16 v140, v140, 0
	v_pk_max_f16 v141, v141, 0
	v_add_u32_e32 v111, s64, v111
	v_add_u32_e32 v98, s65, v98
	s_lshl_b32 s20, s9, 7
	v_lshl_add_u64 v[0:1], s[20:21], 3, v[132:133]
	s_add_i32 s25, s22, s34
	s_lshl_b32 s8, s9, 8
	buffer_load_dwordx4 v[192:195], v147, s[16:19], s25 offen
	buffer_load_dwordx4 v[196:199], v148, s[16:19], s25 offen
	buffer_load_dwordx4 v[200:203], v149, s[16:19], s25 offen
	buffer_load_dwordx4 v[204:207], v150, s[16:19], s25 offen
	s_waitcnt vmcnt(19)
	v_mfma_f32_16x16x32_f16 v[164:167], v[58:61], v[122:125], v[240:243]
	v_cvt_pk_f16_f32 v142, v208, v209
	v_cvt_pk_f16_f32 v143, v210, v211
	v_mfma_f32_16x16x32_f16 v[168:171], v[58:61], v[126:129], v[240:243]
	v_pk_max_f16 v142, v142, 0
	v_pk_max_f16 v143, v143, 0
	ds_write_b128 v107, v[122:125]
	v_mfma_f32_16x16x32_f16 v[172:175], v[58:61], v[134:137], v[240:243]
	v_cvt_pk_f16_f32 v144, v224, v225
	v_cvt_pk_f16_f32 v145, v226, v227
	v_mfma_f32_16x16x32_f16 v[10:13], v[58:61], v[138:141], v[240:243]
	v_pk_max_f16 v144, v144, 0
	v_pk_max_f16 v145, v145, 0
	ds_write_b128 v108, v[142:145]
	s_waitcnt vmcnt(18)
	v_mfma_f32_16x16x32_f16 v[58:61], v[54:57], v[122:125], v[244:247]
	v_cvt_pk_f16_f32 v152, v212, v213
	v_cvt_pk_f16_f32 v153, v214, v215
	v_mfma_f32_16x16x32_f16 v[176:179], v[54:57], v[126:129], v[244:247]
	v_pk_max_f16 v152, v152, 0
	v_pk_max_f16 v153, v153, 0
	ds_write_b128 v107, v[126:129] offset:16384
	v_mfma_f32_16x16x32_f16 v[180:183], v[54:57], v[134:137], v[244:247]
	v_cvt_pk_f16_f32 v154, v228, v229
	v_cvt_pk_f16_f32 v155, v230, v231
	v_mfma_f32_16x16x32_f16 v[18:21], v[54:57], v[138:141], v[244:247]
	v_pk_max_f16 v154, v154, 0
	v_pk_max_f16 v155, v155, 0
	ds_write_b128 v108, v[152:155] offset:16384
	s_waitcnt vmcnt(17)
	v_mfma_f32_16x16x32_f16 v[54:57], v[50:53], v[122:125], v[248:251]
	v_cvt_pk_f16_f32 v156, v216, v217
	v_cvt_pk_f16_f32 v157, v218, v219
	v_mfma_f32_16x16x32_f16 v[184:187], v[50:53], v[126:129], v[248:251]
	v_pk_max_f16 v156, v156, 0
	v_pk_max_f16 v157, v157, 0
	ds_write_b128 v107, v[134:137] offset:32768
	v_mfma_f32_16x16x32_f16 v[188:191], v[50:53], v[134:137], v[248:251]
	v_cvt_pk_f16_f32 v158, v232, v233
	v_cvt_pk_f16_f32 v159, v234, v235
	v_mfma_f32_16x16x32_f16 v[22:25], v[50:53], v[138:141], v[248:251]
	v_pk_max_f16 v158, v158, 0
	v_pk_max_f16 v159, v159, 0
	ds_write_b128 v108, v[156:159] offset:32768
	s_waitcnt vmcnt(16)
	v_mfma_f32_16x16x32_f16 v[50:53], v[38:41], v[122:125], v[252:255]
	v_cvt_pk_f16_f32 v160, v220, v221
	v_cvt_pk_f16_f32 v161, v222, v223
	v_mfma_f32_16x16x32_f16 v[122:125], v[38:41], v[126:129], v[252:255]
	v_pk_max_f16 v160, v160, 0
	v_pk_max_f16 v161, v161, 0
	ds_write_b128 v107, v[138:141] offset:49152
	v_mfma_f32_16x16x32_f16 v[126:129], v[38:41], v[134:137], v[252:255]
	v_cvt_pk_f16_f32 v162, v236, v237
	v_cvt_pk_f16_f32 v163, v238, v239
	v_mfma_f32_16x16x32_f16 v[38:41], v[38:41], v[138:141], v[252:255]
	v_pk_max_f16 v162, v162, 0
	v_pk_max_f16 v163, v163, 0
	ds_write_b128 v108, v[160:163] offset:49152
	s_add_i32 s9, s22, s35
	s_waitcnt vmcnt(15)
	v_mfma_f32_16x16x32_f16 v[164:167], v[94:97], v[142:145], v[164:167]
	v_mfma_f32_16x16x32_f16 v[168:171], v[94:97], v[152:155], v[168:171]
	s_waitcnt vmcnt(14)
	v_mfma_f32_16x16x32_f16 v[58:61], v[90:93], v[142:145], v[58:61]
	v_mfma_f32_16x16x32_f16 v[176:179], v[90:93], v[152:155], v[176:179]
	s_waitcnt vmcnt(13)
	v_mfma_f32_16x16x32_f16 v[54:57], v[78:81], v[142:145], v[54:57]
	v_mfma_f32_16x16x32_f16 v[184:187], v[78:81], v[152:155], v[184:187]
	s_waitcnt vmcnt(12)
	v_mfma_f32_16x16x32_f16 v[50:53], v[34:37], v[142:145], v[50:53]
	buffer_load_dwordx4 v[140:143], v147, s[16:19], s9 offen
	buffer_load_dwordx4 v[220:223], v148, s[16:19], s9 offen
	v_mfma_f32_16x16x32_f16 v[122:125], v[34:37], v[152:155], v[122:125]
	buffer_load_dwordx4 v[152:155], v149, s[16:19], s9 offen
	buffer_load_dwordx4 v[224:227], v150, s[16:19], s9 offen
	s_mov_b32 s9, s21
	s_waitcnt lgkmcnt(0)
	s_barrier
	v_add_u32_e32 v99, s66, v99
	ds_read_b128 v[136:139], v99
	ds_read_b128 v[208:211], v99 offset:16384
	ds_read_b128 v[212:215], v99 offset:32768
	ds_read_b128 v[216:219], v99 offset:49152
	v_mfma_f32_16x16x32_f16 v[172:175], v[94:97], v[156:159], v[172:175]
	v_mfma_f32_16x16x32_f16 v[94:97], v[94:97], v[160:163], v[10:13]
	s_nop 2
	v_lshl_add_u64 v[10:11], s[8:9], 4, v[130:131]
	v_mfma_f32_16x16x32_f16 v[180:183], v[90:93], v[156:159], v[180:183]
	v_mfma_f32_16x16x32_f16 v[90:93], v[90:93], v[160:163], v[18:21]
	v_mfma_f32_16x16x32_f16 v[188:191], v[78:81], v[156:159], v[188:191]
	v_mfma_f32_16x16x32_f16 v[78:81], v[78:81], v[160:163], v[22:25]
	global_load_dwordx4 v[30:33], v[10:11], off
	s_nop 1
	global_load_dwordx4 v[22:25], v[10:11], off offset:1024
	global_load_dwordx4 v[18:21], v[10:11], off offset:2048
	s_nop 0
	global_load_dwordx4 v[10:13], v[10:11], off offset:3072
	s_nop 0
	global_load_dwordx2 v[134:135], v[0:1], off
	v_mfma_f32_16x16x32_f16 v[126:129], v[34:37], v[156:159], v[126:129]
	v_mfma_f32_16x16x32_f16 v[34:37], v[34:37], v[160:163], v[38:41]
	s_nop 2
	v_add_u32_e32 v100, s67, v100
	ds_read_b128 v[38:41], v100
	ds_read_b128 v[156:159], v100 offset:16384
	ds_read_b128 v[160:163], v100 offset:32768
	ds_read_b128 v[228:231], v100 offset:49152
	s_add_i32 s8, s22, s36
	s_waitcnt vmcnt(20) lgkmcnt(7)
	v_mfma_f32_16x16x32_f16 v[164:167], v[82:85], v[136:139], v[164:167]
	s_waitcnt lgkmcnt(6)
	v_mfma_f32_16x16x32_f16 v[168:171], v[82:85], v[208:211], v[168:171]
	s_waitcnt lgkmcnt(5)
	v_mfma_f32_16x16x32_f16 v[172:175], v[82:85], v[212:215], v[172:175]
	s_waitcnt lgkmcnt(4)
	v_mfma_f32_16x16x32_f16 v[82:85], v[82:85], v[216:219], v[94:97]
	s_waitcnt vmcnt(19)
	v_mfma_f32_16x16x32_f16 v[58:61], v[70:73], v[136:139], v[58:61]
	v_mfma_f32_16x16x32_f16 v[94:97], v[70:73], v[208:211], v[176:179]
	v_mfma_f32_16x16x32_f16 v[176:179], v[70:73], v[212:215], v[180:183]
	v_mfma_f32_16x16x32_f16 v[70:73], v[70:73], v[216:219], v[90:93]
	s_waitcnt vmcnt(18)
	v_mfma_f32_16x16x32_f16 v[54:57], v[62:65], v[136:139], v[54:57]
	v_mfma_f32_16x16x32_f16 v[90:93], v[62:65], v[208:211], v[184:187]
	v_mfma_f32_16x16x32_f16 v[180:183], v[62:65], v[212:215], v[188:191]
	v_mfma_f32_16x16x32_f16 v[62:65], v[62:65], v[216:219], v[78:81]
	s_waitcnt vmcnt(17)
	v_mfma_f32_16x16x32_f16 v[50:53], v[42:45], v[136:139], v[50:53]
	v_mfma_f32_16x16x32_f16 v[78:81], v[42:45], v[208:211], v[122:125]
	v_mfma_f32_16x16x32_f16 v[122:125], v[42:45], v[212:215], v[126:129]
	s_nop 2
	buffer_load_dwordx4 v[126:129], v147, s[16:19], s8 offen
	buffer_load_dwordx4 v[136:139], v148, s[16:19], s8 offen
	buffer_load_dwordx4 v[184:187], v149, s[16:19], s8 offen
	buffer_load_dwordx4 v[188:191], v150, s[16:19], s8 offen
	v_mfma_f32_16x16x32_f16 v[34:37], v[42:45], v[216:219], v[34:37]
	v_add_u32_e32 v111, s68, v111
	ds_read_b128 v[42:45], v111
	ds_read_b128 v[208:211], v111 offset:16384
	ds_read_b128 v[212:215], v111 offset:32768
	ds_read_b128 v[216:219], v111 offset:49152
	s_add_i32 s8, s22, s37
	s_waitcnt vmcnt(20) lgkmcnt(7)
	v_mfma_f32_16x16x32_f16 v[164:167], v[86:89], v[38:41], v[164:167]
	s_waitcnt lgkmcnt(6)
	v_mfma_f32_16x16x32_f16 v[168:171], v[86:89], v[156:159], v[168:171]
	s_waitcnt lgkmcnt(5)
	v_mfma_f32_16x16x32_f16 v[172:175], v[86:89], v[160:163], v[172:175]
	s_waitcnt lgkmcnt(4)
	v_mfma_f32_16x16x32_f16 v[82:85], v[86:89], v[228:231], v[82:85]
	s_waitcnt vmcnt(19)
	v_mfma_f32_16x16x32_f16 v[58:61], v[74:77], v[38:41], v[58:61]
	v_mfma_f32_16x16x32_f16 v[86:89], v[74:77], v[156:159], v[94:97]
	v_mfma_f32_16x16x32_f16 v[94:97], v[74:77], v[160:163], v[176:179]
	v_mfma_f32_16x16x32_f16 v[70:73], v[74:77], v[228:231], v[70:73]
	s_waitcnt vmcnt(18)
	v_mfma_f32_16x16x32_f16 v[54:57], v[66:69], v[38:41], v[54:57]
	v_mfma_f32_16x16x32_f16 v[74:77], v[66:69], v[156:159], v[90:93]
	v_mfma_f32_16x16x32_f16 v[90:93], v[66:69], v[160:163], v[180:183]
	v_mfma_f32_16x16x32_f16 v[62:65], v[66:69], v[228:231], v[62:65]
	s_waitcnt vmcnt(17)
	v_mfma_f32_16x16x32_f16 v[38:41], v[46:49], v[38:41], v[50:53]
	v_mfma_f32_16x16x32_f16 v[50:53], v[46:49], v[156:159], v[78:81]
	v_mfma_f32_16x16x32_f16 v[66:69], v[46:49], v[160:163], v[122:125]
	s_nop 1
	buffer_load_dwordx4 v[78:81], v147, s[16:19], s8 offen
	buffer_load_dwordx4 v[122:125], v148, s[16:19], s8 offen
	buffer_load_dwordx4 v[156:159], v149, s[16:19], s8 offen
	buffer_load_dwordx4 v[160:163], v150, s[16:19], s8 offen
	v_mfma_f32_16x16x32_f16 v[34:37], v[46:49], v[228:231], v[34:37]
	v_add_u32_e32 v98, s69, v98
	ds_read_b128 v[46:49], v98
	ds_read_b128 v[176:179], v98 offset:16384
	ds_read_b128 v[180:183], v98 offset:32768
	ds_read_b128 v[228:231], v98 offset:49152
	s_add_i32 s8, s22, s38
	s_waitcnt vmcnt(20) lgkmcnt(7)
	v_mfma_f32_16x16x32_f16 v[164:167], v[192:195], v[42:45], v[164:167]
	s_waitcnt lgkmcnt(6)
	v_mfma_f32_16x16x32_f16 v[168:171], v[192:195], v[208:211], v[168:171]
	s_waitcnt lgkmcnt(5)
	v_mfma_f32_16x16x32_f16 v[172:175], v[192:195], v[212:215], v[172:175]
	s_waitcnt lgkmcnt(4)
	v_mfma_f32_16x16x32_f16 v[82:85], v[192:195], v[216:219], v[82:85]
	s_waitcnt vmcnt(19)
	v_mfma_f32_16x16x32_f16 v[58:61], v[196:199], v[42:45], v[58:61]
	v_mfma_f32_16x16x32_f16 v[86:89], v[196:199], v[208:211], v[86:89]
	v_mfma_f32_16x16x32_f16 v[94:97], v[196:199], v[212:215], v[94:97]
	v_mfma_f32_16x16x32_f16 v[70:73], v[196:199], v[216:219], v[70:73]
	s_waitcnt vmcnt(18)
	v_mfma_f32_16x16x32_f16 v[54:57], v[200:203], v[42:45], v[54:57]
	v_mfma_f32_16x16x32_f16 v[74:77], v[200:203], v[208:211], v[74:77]
	v_mfma_f32_16x16x32_f16 v[90:93], v[200:203], v[212:215], v[90:93]
	v_mfma_f32_16x16x32_f16 v[62:65], v[200:203], v[216:219], v[62:65]
	s_waitcnt vmcnt(17)
	v_mfma_f32_16x16x32_f16 v[38:41], v[204:207], v[42:45], v[38:41]
	v_mfma_f32_16x16x32_f16 v[42:45], v[204:207], v[208:211], v[50:53]
	v_mfma_f32_16x16x32_f16 v[50:53], v[204:207], v[212:215], v[66:69]
	s_nop 2
	buffer_load_dwordx4 v[66:69], v147, s[16:19], s8 offen
	buffer_load_dwordx4 v[192:195], v148, s[16:19], s8 offen
	buffer_load_dwordx4 v[196:199], v149, s[16:19], s8 offen
	buffer_load_dwordx4 v[200:203], v150, s[16:19], s8 offen
	v_mfma_f32_16x16x32_f16 v[34:37], v[204:207], v[216:219], v[34:37]
	v_add_u32_e32 v99, s70, v99
	ds_read_b128 v[204:207], v99
	ds_read_b128 v[208:211], v99 offset:16384
	ds_read_b128 v[212:215], v99 offset:32768
	ds_read_b128 v[216:219], v99 offset:49152
	s_add_i32 s8, s22, s39
	s_waitcnt vmcnt(20) lgkmcnt(7)
	v_mfma_f32_16x16x32_f16 v[164:167], v[140:143], v[46:49], v[164:167]
	s_waitcnt lgkmcnt(6)
	v_mfma_f32_16x16x32_f16 v[168:171], v[140:143], v[176:179], v[168:171]
	s_waitcnt lgkmcnt(5)
	v_mfma_f32_16x16x32_f16 v[172:175], v[140:143], v[180:183], v[172:175]
	s_waitcnt lgkmcnt(4)
	v_mfma_f32_16x16x32_f16 v[82:85], v[140:143], v[228:231], v[82:85]
	s_waitcnt vmcnt(19)
	v_mfma_f32_16x16x32_f16 v[58:61], v[220:223], v[46:49], v[58:61]
	v_mfma_f32_16x16x32_f16 v[86:89], v[220:223], v[176:179], v[86:89]
	s_waitcnt vmcnt(18)
	v_mfma_f32_16x16x32_f16 v[54:57], v[152:155], v[46:49], v[54:57]
	v_mfma_f32_16x16x32_f16 v[74:77], v[152:155], v[176:179], v[74:77]
	v_mfma_f32_16x16x32_f16 v[90:93], v[152:155], v[180:183], v[90:93]
	v_mfma_f32_16x16x32_f16 v[62:65], v[152:155], v[228:231], v[62:65]
	s_waitcnt vmcnt(17)
	v_mfma_f32_16x16x32_f16 v[38:41], v[224:227], v[46:49], v[38:41]
	v_mfma_f32_16x16x32_f16 v[42:45], v[224:227], v[176:179], v[42:45]
	v_mfma_f32_16x16x32_f16 v[46:49], v[224:227], v[180:183], v[50:53]
	s_nop 2
	buffer_load_dwordx4 v[50:53], v147, s[16:19], s8 offen
	buffer_load_dwordx4 v[140:143], v148, s[16:19], s8 offen
	buffer_load_dwordx4 v[152:155], v149, s[16:19], s8 offen
	buffer_load_dwordx4 v[176:179], v150, s[16:19], s8 offen
	v_mfma_f32_16x16x32_f16 v[94:97], v[220:223], v[180:183], v[94:97]
	v_mfma_f32_16x16x32_f16 v[70:73], v[220:223], v[228:231], v[70:73]
	v_mfma_f32_16x16x32_f16 v[34:37], v[224:227], v[228:231], v[34:37]
	v_add_u32_e32 v100, s71, v100
	ds_read_b128 v[180:183], v100
	ds_read_b128 v[220:223], v100 offset:16384
	ds_read_b128 v[224:227], v100 offset:32768
	ds_read_b128 v[228:231], v100 offset:49152
	s_add_i32 s8, s22, s40
	s_waitcnt vmcnt(15) lgkmcnt(7)
	v_mfma_f32_16x16x32_f16 v[164:167], v[126:129], v[204:207], v[164:167]
	s_waitcnt lgkmcnt(6)
	v_mfma_f32_16x16x32_f16 v[168:171], v[126:129], v[208:211], v[168:171]
	s_waitcnt lgkmcnt(5)
	v_mfma_f32_16x16x32_f16 v[172:175], v[126:129], v[212:215], v[172:175]
	s_waitcnt lgkmcnt(4)
	v_mfma_f32_16x16x32_f16 v[82:85], v[126:129], v[216:219], v[82:85]
	s_waitcnt vmcnt(14)
	v_mfma_f32_16x16x32_f16 v[58:61], v[136:139], v[204:207], v[58:61]
	v_mfma_f32_16x16x32_f16 v[86:89], v[136:139], v[208:211], v[86:89]
	v_mfma_f32_16x16x32_f16 v[94:97], v[136:139], v[212:215], v[94:97]
	v_mfma_f32_16x16x32_f16 v[70:73], v[136:139], v[216:219], v[70:73]
	s_waitcnt vmcnt(13)
	v_mfma_f32_16x16x32_f16 v[54:57], v[184:187], v[204:207], v[54:57]
	v_mfma_f32_16x16x32_f16 v[74:77], v[184:187], v[208:211], v[74:77]
	v_mfma_f32_16x16x32_f16 v[90:93], v[184:187], v[212:215], v[90:93]
	v_mfma_f32_16x16x32_f16 v[62:65], v[184:187], v[216:219], v[62:65]
	s_waitcnt vmcnt(12)
	v_mfma_f32_16x16x32_f16 v[38:41], v[188:191], v[204:207], v[38:41]
	buffer_load_dwordx4 v[126:129], v147, s[16:19], s8 offen
	buffer_load_dwordx4 v[136:139], v148, s[16:19], s8 offen
	buffer_load_dwordx4 v[184:187], v149, s[16:19], s8 offen
	buffer_load_dwordx4 v[204:207], v150, s[16:19], s8 offen
	v_mfma_f32_16x16x32_f16 v[42:45], v[188:191], v[208:211], v[42:45]
	v_mfma_f32_16x16x32_f16 v[46:49], v[188:191], v[212:215], v[46:49]
	v_mfma_f32_16x16x32_f16 v[34:37], v[188:191], v[216:219], v[34:37]
	v_add_u32_e32 v111, s72, v111
	ds_read_b128 v[188:191], v111
	ds_read_b128 v[208:211], v111 offset:16384
	ds_read_b128 v[212:215], v111 offset:32768
	ds_read_b128 v[216:219], v111 offset:49152
	s_add_i32 s8, s22, s41
	s_waitcnt vmcnt(15) lgkmcnt(7)
	v_mfma_f32_16x16x32_f16 v[164:167], v[78:81], v[180:183], v[164:167]
	s_waitcnt lgkmcnt(6)
	v_mfma_f32_16x16x32_f16 v[168:171], v[78:81], v[220:223], v[168:171]
	s_waitcnt lgkmcnt(5)
	v_mfma_f32_16x16x32_f16 v[172:175], v[78:81], v[224:227], v[172:175]
	s_waitcnt lgkmcnt(4)
	v_mfma_f32_16x16x32_f16 v[78:81], v[78:81], v[228:231], v[82:85]
	s_waitcnt vmcnt(14)
	v_mfma_f32_16x16x32_f16 v[58:61], v[122:125], v[180:183], v[58:61]
	v_mfma_f32_16x16x32_f16 v[82:85], v[122:125], v[220:223], v[86:89]
	v_mfma_f32_16x16x32_f16 v[86:89], v[122:125], v[224:227], v[94:97]
	v_mfma_f32_16x16x32_f16 v[70:73], v[122:125], v[228:231], v[70:73]
	s_waitcnt vmcnt(13)
	v_mfma_f32_16x16x32_f16 v[54:57], v[156:159], v[180:183], v[54:57]
	v_mfma_f32_16x16x32_f16 v[74:77], v[156:159], v[220:223], v[74:77]
	v_mfma_f32_16x16x32_f16 v[90:93], v[156:159], v[224:227], v[90:93]
	v_mfma_f32_16x16x32_f16 v[62:65], v[156:159], v[228:231], v[62:65]
	s_waitcnt vmcnt(12)
	v_mfma_f32_16x16x32_f16 v[38:41], v[160:163], v[180:183], v[38:41]
	buffer_load_dwordx4 v[94:97], v147, s[16:19], s8 offen
	buffer_load_dwordx4 v[122:125], v148, s[16:19], s8 offen
	buffer_load_dwordx4 v[156:159], v149, s[16:19], s8 offen
	buffer_load_dwordx4 v[180:183], v150, s[16:19], s8 offen
	v_mfma_f32_16x16x32_f16 v[42:45], v[160:163], v[220:223], v[42:45]
	v_mfma_f32_16x16x32_f16 v[46:49], v[160:163], v[224:227], v[46:49]
	v_mfma_f32_16x16x32_f16 v[34:37], v[160:163], v[228:231], v[34:37]
	v_add_u32_e32 v98, s73, v98
	ds_read_b128 v[160:163], v98
	ds_read_b128 v[220:223], v98 offset:16384
	ds_read_b128 v[224:227], v98 offset:32768
	ds_read_b128 v[228:231], v98 offset:49152
	s_add_i32 s8, s22, s42
	s_waitcnt vmcnt(15) lgkmcnt(7)
	v_mfma_f32_16x16x32_f16 v[164:167], v[66:69], v[188:191], v[164:167]
	s_waitcnt lgkmcnt(6)
	v_mfma_f32_16x16x32_f16 v[168:171], v[66:69], v[208:211], v[168:171]
	s_waitcnt lgkmcnt(5)
	v_mfma_f32_16x16x32_f16 v[172:175], v[66:69], v[212:215], v[172:175]
	s_waitcnt lgkmcnt(4)
	v_mfma_f32_16x16x32_f16 v[66:69], v[66:69], v[216:219], v[78:81]
	s_waitcnt vmcnt(14)
	v_mfma_f32_16x16x32_f16 v[58:61], v[192:195], v[188:191], v[58:61]
	v_mfma_f32_16x16x32_f16 v[78:81], v[192:195], v[208:211], v[82:85]
	v_mfma_f32_16x16x32_f16 v[82:85], v[192:195], v[212:215], v[86:89]
	v_mfma_f32_16x16x32_f16 v[70:73], v[192:195], v[216:219], v[70:73]
	s_waitcnt vmcnt(13)
	v_mfma_f32_16x16x32_f16 v[54:57], v[196:199], v[188:191], v[54:57]
	v_mfma_f32_16x16x32_f16 v[74:77], v[196:199], v[208:211], v[74:77]
	v_mfma_f32_16x16x32_f16 v[86:89], v[196:199], v[212:215], v[90:93]
	v_mfma_f32_16x16x32_f16 v[62:65], v[196:199], v[216:219], v[62:65]
	s_waitcnt vmcnt(12)
	v_mfma_f32_16x16x32_f16 v[38:41], v[200:203], v[188:191], v[38:41]
	buffer_load_dwordx4 v[90:93], v147, s[16:19], s8 offen
	buffer_load_dwordx4 v[188:191], v148, s[16:19], s8 offen
	buffer_load_dwordx4 v[192:195], v149, s[16:19], s8 offen
	buffer_load_dwordx4 v[196:199], v150, s[16:19], s8 offen
	v_mfma_f32_16x16x32_f16 v[42:45], v[200:203], v[208:211], v[42:45]
	v_mfma_f32_16x16x32_f16 v[46:49], v[200:203], v[212:215], v[46:49]
	v_mfma_f32_16x16x32_f16 v[34:37], v[200:203], v[216:219], v[34:37]
	v_add_u32_e32 v99, s74, v99
	ds_read_b128 v[200:203], v99
	ds_read_b128 v[208:211], v99 offset:16384
	ds_read_b128 v[212:215], v99 offset:32768
	ds_read_b128 v[216:219], v99 offset:49152
	s_add_i32 s8, s22, s43
	s_waitcnt vmcnt(15) lgkmcnt(7)
	v_mfma_f32_16x16x32_f16 v[164:167], v[50:53], v[160:163], v[164:167]
	s_waitcnt lgkmcnt(6)
	v_mfma_f32_16x16x32_f16 v[168:171], v[50:53], v[220:223], v[168:171]
	s_waitcnt lgkmcnt(5)
	v_mfma_f32_16x16x32_f16 v[172:175], v[50:53], v[224:227], v[172:175]
	s_waitcnt lgkmcnt(4)
	v_mfma_f32_16x16x32_f16 v[50:53], v[50:53], v[228:231], v[66:69]
	s_waitcnt vmcnt(14)
	v_mfma_f32_16x16x32_f16 v[58:61], v[140:143], v[160:163], v[58:61]
	v_mfma_f32_16x16x32_f16 v[66:69], v[140:143], v[220:223], v[78:81]
	v_mfma_f32_16x16x32_f16 v[78:81], v[140:143], v[224:227], v[82:85]
	v_mfma_f32_16x16x32_f16 v[70:73], v[140:143], v[228:231], v[70:73]
	s_waitcnt vmcnt(13)
	v_mfma_f32_16x16x32_f16 v[54:57], v[152:155], v[160:163], v[54:57]
	v_mfma_f32_16x16x32_f16 v[74:77], v[152:155], v[220:223], v[74:77]
	v_mfma_f32_16x16x32_f16 v[82:85], v[152:155], v[224:227], v[86:89]
	v_mfma_f32_16x16x32_f16 v[62:65], v[152:155], v[228:231], v[62:65]
	s_waitcnt vmcnt(12)
	v_mfma_f32_16x16x32_f16 v[38:41], v[176:179], v[160:163], v[38:41]
	buffer_load_dwordx4 v[86:89], v147, s[16:19], s8 offen
	buffer_load_dwordx4 v[140:143], v148, s[16:19], s8 offen
	buffer_load_dwordx4 v[152:155], v149, s[16:19], s8 offen
	buffer_load_dwordx4 v[160:163], v150, s[16:19], s8 offen
	v_mfma_f32_16x16x32_f16 v[42:45], v[176:179], v[220:223], v[42:45]
	v_mfma_f32_16x16x32_f16 v[46:49], v[176:179], v[224:227], v[46:49]
	v_mfma_f32_16x16x32_f16 v[34:37], v[176:179], v[228:231], v[34:37]
	v_add_u32_e32 v100, s75, v100
	ds_read_b128 v[176:179], v100
	ds_read_b128 v[220:223], v100 offset:16384
	ds_read_b128 v[224:227], v100 offset:32768
	ds_read_b128 v[228:231], v100 offset:49152
	s_add_i32 s8, s22, s44
	s_waitcnt vmcnt(15) lgkmcnt(7)
	v_mfma_f32_16x16x32_f16 v[164:167], v[126:129], v[200:203], v[164:167]
	s_waitcnt lgkmcnt(6)
	v_mfma_f32_16x16x32_f16 v[168:171], v[126:129], v[208:211], v[168:171]
	s_waitcnt lgkmcnt(5)
	v_mfma_f32_16x16x32_f16 v[172:175], v[126:129], v[212:215], v[172:175]
	s_waitcnt lgkmcnt(4)
	v_mfma_f32_16x16x32_f16 v[50:53], v[126:129], v[216:219], v[50:53]
	s_waitcnt vmcnt(14)
	v_mfma_f32_16x16x32_f16 v[58:61], v[136:139], v[200:203], v[58:61]
	v_mfma_f32_16x16x32_f16 v[66:69], v[136:139], v[208:211], v[66:69]
	v_mfma_f32_16x16x32_f16 v[78:81], v[136:139], v[212:215], v[78:81]
	v_mfma_f32_16x16x32_f16 v[70:73], v[136:139], v[216:219], v[70:73]
	s_waitcnt vmcnt(13)
	v_mfma_f32_16x16x32_f16 v[54:57], v[184:187], v[200:203], v[54:57]
	v_mfma_f32_16x16x32_f16 v[74:77], v[184:187], v[208:211], v[74:77]
	v_mfma_f32_16x16x32_f16 v[82:85], v[184:187], v[212:215], v[82:85]
	v_mfma_f32_16x16x32_f16 v[62:65], v[184:187], v[216:219], v[62:65]
	s_waitcnt vmcnt(12)
	v_mfma_f32_16x16x32_f16 v[38:41], v[204:207], v[200:203], v[38:41]
	buffer_load_dwordx4 v[126:129], v147, s[16:19], s8 offen
	buffer_load_dwordx4 v[136:139], v148, s[16:19], s8 offen
	buffer_load_dwordx4 v[184:187], v149, s[16:19], s8 offen
	buffer_load_dwordx4 v[200:203], v150, s[16:19], s8 offen
	v_mfma_f32_16x16x32_f16 v[42:45], v[204:207], v[208:211], v[42:45]
	v_mfma_f32_16x16x32_f16 v[46:49], v[204:207], v[212:215], v[46:49]
	v_mfma_f32_16x16x32_f16 v[34:37], v[204:207], v[216:219], v[34:37]
	v_add_u32_e32 v111, s76, v111
	ds_read_b128 v[204:207], v111
	ds_read_b128 v[208:211], v111 offset:16384
	ds_read_b128 v[212:215], v111 offset:32768
	ds_read_b128 v[216:219], v111 offset:49152
	s_add_i32 s8, s22, s45
	s_waitcnt vmcnt(15) lgkmcnt(7)
	v_mfma_f32_16x16x32_f16 v[164:167], v[94:97], v[176:179], v[164:167]
	s_waitcnt lgkmcnt(6)
	v_mfma_f32_16x16x32_f16 v[168:171], v[94:97], v[220:223], v[168:171]
	s_waitcnt vmcnt(14)
	v_mfma_f32_16x16x32_f16 v[58:61], v[122:125], v[176:179], v[58:61]
	v_mfma_f32_16x16x32_f16 v[66:69], v[122:125], v[220:223], v[66:69]
	s_waitcnt lgkmcnt(5)
	v_mfma_f32_16x16x32_f16 v[78:81], v[122:125], v[224:227], v[78:81]
	s_waitcnt lgkmcnt(4)
	v_mfma_f32_16x16x32_f16 v[70:73], v[122:125], v[228:231], v[70:73]
	s_waitcnt vmcnt(13)
	v_mfma_f32_16x16x32_f16 v[54:57], v[156:159], v[176:179], v[54:57]
	v_mfma_f32_16x16x32_f16 v[74:77], v[156:159], v[220:223], v[74:77]
	v_mfma_f32_16x16x32_f16 v[82:85], v[156:159], v[224:227], v[82:85]
	v_mfma_f32_16x16x32_f16 v[62:65], v[156:159], v[228:231], v[62:65]
	s_waitcnt vmcnt(12)
	v_mfma_f32_16x16x32_f16 v[38:41], v[180:183], v[176:179], v[38:41]
	v_mfma_f32_16x16x32_f16 v[42:45], v[180:183], v[220:223], v[42:45]
	buffer_load_dwordx4 v[122:125], v147, s[16:19], s8 offen
	buffer_load_dwordx4 v[156:159], v148, s[16:19], s8 offen
	buffer_load_dwordx4 v[176:179], v149, s[16:19], s8 offen
	buffer_load_dwordx4 v[220:223], v150, s[16:19], s8 offen
	v_mfma_f32_16x16x32_f16 v[50:53], v[94:97], v[228:231], v[50:53]
	v_mfma_f32_16x16x32_f16 v[46:49], v[180:183], v[224:227], v[46:49]
	v_mfma_f32_16x16x32_f16 v[34:37], v[180:183], v[228:231], v[34:37]
	v_mfma_f32_16x16x32_f16 v[172:175], v[94:97], v[224:227], v[172:175]
	v_add_u32_e32 v98, s77, v98
	ds_read_b128 v[94:97], v98
	ds_read_b128 v[180:183], v98 offset:16384
	ds_read_b128 v[224:227], v98 offset:32768
	ds_read_b128 v[228:231], v98 offset:49152
	s_add_i32 s8, s22, s46
	s_waitcnt vmcnt(15) lgkmcnt(7)
	v_mfma_f32_16x16x32_f16 v[164:167], v[90:93], v[204:207], v[164:167]
	s_waitcnt lgkmcnt(6)
	v_mfma_f32_16x16x32_f16 v[168:171], v[90:93], v[208:211], v[168:171]
	s_waitcnt lgkmcnt(5)
	v_mfma_f32_16x16x32_f16 v[172:175], v[90:93], v[212:215], v[172:175]
	s_waitcnt lgkmcnt(4)
	v_mfma_f32_16x16x32_f16 v[90:93], v[90:93], v[216:219], v[50:53]
	s_waitcnt vmcnt(14)
	v_mfma_f32_16x16x32_f16 v[232:235], v[188:191], v[204:207], v[58:61]
	v_mfma_f32_16x16x32_f16 v[66:69], v[188:191], v[208:211], v[66:69]
	v_mfma_f32_16x16x32_f16 v[78:81], v[188:191], v[212:215], v[78:81]
	v_mfma_f32_16x16x32_f16 v[70:73], v[188:191], v[216:219], v[70:73]
	s_waitcnt vmcnt(13)
	v_mfma_f32_16x16x32_f16 v[188:191], v[192:195], v[204:207], v[54:57]
	v_mfma_f32_16x16x32_f16 v[74:77], v[192:195], v[208:211], v[74:77]
	v_mfma_f32_16x16x32_f16 v[82:85], v[192:195], v[212:215], v[82:85]
	v_mfma_f32_16x16x32_f16 v[62:65], v[192:195], v[216:219], v[62:65]
	s_waitcnt vmcnt(12)
	v_mfma_f32_16x16x32_f16 v[192:195], v[196:199], v[204:207], v[38:41]
	buffer_load_dwordx4 v[58:61], v147, s[16:19], s8 offen
	buffer_load_dwordx4 v[54:57], v148, s[16:19], s8 offen
	buffer_load_dwordx4 v[50:53], v149, s[16:19], s8 offen
	buffer_load_dwordx4 v[38:41], v150, s[16:19], s8 offen
	v_mfma_f32_16x16x32_f16 v[42:45], v[196:199], v[208:211], v[42:45]
	v_mfma_f32_16x16x32_f16 v[46:49], v[196:199], v[212:215], v[46:49]
	v_mfma_f32_16x16x32_f16 v[196:199], v[196:199], v[216:219], v[34:37]
	v_add_u32_e32 v99, s78, v99
	ds_read_b128 v[204:207], v99
	ds_read_b128 v[208:211], v99 offset:16384
	ds_read_b128 v[212:215], v99 offset:32768
	ds_read_b128 v[216:219], v99 offset:49152
	s_add_i32 s8, s22, s47
	s_waitcnt vmcnt(15) lgkmcnt(7)
	v_mfma_f32_16x16x32_f16 v[164:167], v[86:89], v[94:97], v[164:167]
	s_waitcnt lgkmcnt(6)
	v_mfma_f32_16x16x32_f16 v[168:171], v[86:89], v[180:183], v[168:171]
	s_waitcnt lgkmcnt(5)
	v_mfma_f32_16x16x32_f16 v[172:175], v[86:89], v[224:227], v[172:175]
	s_waitcnt lgkmcnt(4)
	v_mfma_f32_16x16x32_f16 v[86:89], v[86:89], v[228:231], v[90:93]
	s_waitcnt vmcnt(14)
	v_mfma_f32_16x16x32_f16 v[232:235], v[140:143], v[94:97], v[232:235]
	v_mfma_f32_16x16x32_f16 v[66:69], v[140:143], v[180:183], v[66:69]
	v_mfma_f32_16x16x32_f16 v[236:239], v[140:143], v[224:227], v[78:81]
	v_mfma_f32_16x16x32_f16 v[70:73], v[140:143], v[228:231], v[70:73]
	s_waitcnt vmcnt(13)
	v_mfma_f32_16x16x32_f16 v[140:143], v[152:155], v[94:97], v[188:191]
	v_mfma_f32_16x16x32_f16 v[74:77], v[152:155], v[180:183], v[74:77]
	v_mfma_f32_16x16x32_f16 v[82:85], v[152:155], v[224:227], v[82:85]
	v_mfma_f32_16x16x32_f16 v[62:65], v[152:155], v[228:231], v[62:65]
	s_waitcnt vmcnt(12)
	v_mfma_f32_16x16x32_f16 v[152:155], v[160:163], v[94:97], v[192:195]
	buffer_load_dwordx4 v[94:97], v147, s[16:19], s8 offen
	buffer_load_dwordx4 v[90:93], v148, s[16:19], s8 offen
	buffer_load_dwordx4 v[78:81], v149, s[16:19], s8 offen
	buffer_load_dwordx4 v[34:37], v150, s[16:19], s8 offen
	v_mfma_f32_16x16x32_f16 v[42:45], v[160:163], v[180:183], v[42:45]
	v_mfma_f32_16x16x32_f16 v[46:49], v[160:163], v[224:227], v[46:49]
	v_mfma_f32_16x16x32_f16 v[160:163], v[160:163], v[228:231], v[196:199]
	v_add_u32_e32 v100, s79, v100
	ds_read_b128 v[180:183], v100
	ds_read_b128 v[188:191], v100 offset:16384
	ds_read_b128 v[192:195], v100 offset:32768
	ds_read_b128 v[196:199], v100 offset:49152
	s_add_i32 s8, s22, s48
	s_waitcnt vmcnt(15) lgkmcnt(7)
	v_mfma_f32_16x16x32_f16 v[164:167], v[126:129], v[204:207], v[164:167]
	s_waitcnt lgkmcnt(6)
	v_mfma_f32_16x16x32_f16 v[168:171], v[126:129], v[208:211], v[168:171]
	s_waitcnt lgkmcnt(5)
	v_mfma_f32_16x16x32_f16 v[172:175], v[126:129], v[212:215], v[172:175]
	s_waitcnt lgkmcnt(4)
	v_mfma_f32_16x16x32_f16 v[86:89], v[126:129], v[216:219], v[86:89]
	s_waitcnt vmcnt(14)
	v_mfma_f32_16x16x32_f16 v[126:129], v[136:139], v[204:207], v[232:235]
	v_mfma_f32_16x16x32_f16 v[66:69], v[136:139], v[208:211], v[66:69]
	v_mfma_f32_16x16x32_f16 v[224:227], v[136:139], v[212:215], v[236:239]
	v_mfma_f32_16x16x32_f16 v[136:139], v[136:139], v[216:219], v[70:73]
	s_waitcnt vmcnt(13)
	v_mfma_f32_16x16x32_f16 v[140:143], v[184:187], v[204:207], v[140:143]
	v_mfma_f32_16x16x32_f16 v[74:77], v[184:187], v[208:211], v[74:77]
	v_mfma_f32_16x16x32_f16 v[228:231], v[184:187], v[212:215], v[82:85]
	v_mfma_f32_16x16x32_f16 v[184:187], v[184:187], v[216:219], v[62:65]
	s_waitcnt vmcnt(12)
	v_mfma_f32_16x16x32_f16 v[152:155], v[200:203], v[204:207], v[152:155]
	v_mfma_f32_16x16x32_f16 v[204:207], v[200:203], v[208:211], v[42:45]
	buffer_load_dwordx4 v[82:85], v147, s[16:19], s8 offen
	buffer_load_dwordx4 v[70:73], v148, s[16:19], s8 offen
	buffer_load_dwordx4 v[62:65], v149, s[16:19], s8 offen
	buffer_load_dwordx4 v[42:45], v150, s[16:19], s8 offen
	v_mfma_f32_16x16x32_f16 v[46:49], v[200:203], v[212:215], v[46:49]
	v_mfma_f32_16x16x32_f16 v[160:163], v[200:203], v[216:219], v[160:163]
	v_add_u32_e32 v0, 0x1ac00, v104
	ds_read_b128 v[240:243], v0
	ds_read_b128 v[244:247], v0 offset:16
	s_waitcnt vmcnt(12) lgkmcnt(5)
	v_mfma_f32_16x16x32_f16 v[164:167], v[122:125], v[180:183], v[164:167]
	v_mfma_f32_16x16x32_f16 v[126:129], v[156:159], v[180:183], v[126:129]
	v_mfma_f32_16x16x32_f16 v[140:143], v[176:179], v[180:183], v[140:143]
	v_mfma_f32_16x16x32_f16 v[152:155], v[220:223], v[180:183], v[152:155]
	s_waitcnt lgkmcnt(4)
	v_mfma_f32_16x16x32_f16 v[168:171], v[122:125], v[188:191], v[168:171]
	v_mfma_f32_16x16x32_f16 v[208:211], v[156:159], v[188:191], v[66:69]
	v_mfma_f32_16x16x32_f16 v[212:215], v[176:179], v[188:191], v[74:77]
	v_mfma_f32_16x16x32_f16 v[204:207], v[220:223], v[188:191], v[204:207]
	s_waitcnt lgkmcnt(3)
	v_mfma_f32_16x16x32_f16 v[172:175], v[122:125], v[192:195], v[172:175]
	v_cvt_pk_f16_f32 v232, v164, v165
	v_cvt_pk_f16_f32 v233, v166, v167
	v_pk_max_f16 v232, v232, 0
	v_pk_max_f16 v233, v233, 0
	v_mfma_f32_16x16x32_f16 v[224:227], v[156:159], v[192:195], v[224:227]
	v_cvt_pk_f16_f32 v234, v126, v127
	v_cvt_pk_f16_f32 v235, v128, v129
	v_pk_max_f16 v234, v234, 0
	v_pk_max_f16 v235, v235, 0
	v_mfma_f32_16x16x32_f16 v[228:231], v[176:179], v[192:195], v[228:231]
	v_cvt_pk_f16_f32 v236, v140, v141
	v_cvt_pk_f16_f32 v237, v142, v143
	v_pk_max_f16 v236, v236, 0
	v_pk_max_f16 v237, v237, 0
	v_mfma_f32_16x16x32_f16 v[216:219], v[220:223], v[192:195], v[46:49]
	v_cvt_pk_f16_f32 v238, v152, v153
	v_cvt_pk_f16_f32 v239, v154, v155
	v_pk_max_f16 v238, v238, 0
	v_pk_max_f16 v239, v239, 0
	s_waitcnt lgkmcnt(2)
	v_mfma_f32_16x16x32_f16 v[200:203], v[122:125], v[196:199], v[86:89]
	v_cvt_pk_f16_f32 v180, v168, v169
	v_cvt_pk_f16_f32 v181, v170, v171
	v_pk_max_f16 v180, v180, 0
	v_pk_max_f16 v181, v181, 0
	s_add_i32 s8, s22, s49
	buffer_load_dwordx4 v[86:89], v147, s[16:19], s8 offen
	buffer_load_dwordx4 v[74:77], v148, s[16:19], s8 offen
	buffer_load_dwordx4 v[66:69], v149, s[16:19], s8 offen
	buffer_load_dwordx4 v[46:49], v150, s[16:19], s8 offen
	v_mfma_f32_16x16x32_f16 v[136:139], v[156:159], v[196:199], v[136:139]
	v_cvt_pk_f16_f32 v182, v208, v209
	v_cvt_pk_f16_f32 v183, v210, v211
	v_pk_max_f16 v182, v182, 0
	v_pk_max_f16 v183, v183, 0
	s_waitcnt lgkmcnt(1)
	v_mfma_f32_16x16x32_f16 v[252:255], v[240:243], v[232:235], 0
	v_cvt_pk_f16_f32 v232, v172, v173
	v_cvt_pk_f16_f32 v233, v174, v175
	v_pk_max_f16 v232, v232, 0
	v_pk_max_f16 v233, v233, 0
	v_mfma_f32_16x16x32_f16 v[184:187], v[176:179], v[196:199], v[184:187]
	v_cvt_pk_f16_f32 v188, v212, v213
	v_cvt_pk_f16_f32 v189, v214, v215
	v_pk_max_f16 v188, v188, 0
	v_pk_max_f16 v189, v189, 0
	s_waitcnt lgkmcnt(0)
	v_mfma_f32_16x16x32_f16 v[252:255], v[244:247], v[236:239], v[252:255]
	ds_read_u16 v102, v114
	ds_read_u16 v103, v114 offset:512
	ds_read_u16 v115, v114 offset:1024
	ds_read_u16 v116, v114 offset:1536
	v_cvt_pk_f16_f32 v234, v224, v225
	v_cvt_pk_f16_f32 v235, v226, v227
	v_pk_max_f16 v234, v234, 0
	v_pk_max_f16 v235, v235, 0
	v_mfma_f32_16x16x32_f16 v[160:163], v[220:223], v[196:199], v[160:163]
	v_cvt_pk_f16_f32 v190, v204, v205
	v_cvt_pk_f16_f32 v191, v206, v207
	v_pk_max_f16 v190, v190, 0
	v_pk_max_f16 v191, v191, 0
	v_mfma_f32_16x16x32_f16 v[192:195], v[240:243], v[180:183], 0
	v_cvt_pk_f16_f32 v236, v228, v229
	v_cvt_pk_f16_f32 v237, v230, v231
	v_pk_max_f16 v236, v236, 0
	v_pk_max_f16 v237, v237, 0
	v_mfma_f32_16x16x32_f16 v[192:195], v[244:247], v[188:191], v[192:195]
	v_cvt_pk_f16_f32 v238, v216, v217
	v_cvt_pk_f16_f32 v239, v218, v219
	v_pk_max_f16 v238, v238, 0
	v_pk_max_f16 v239, v239, 0
	v_cvt_pk_f16_f32 v180, v200, v201
	v_cvt_pk_f16_f32 v181, v202, v203
	v_pk_max_f16 v180, v180, 0
	v_pk_max_f16 v181, v181, 0
	v_mfma_f32_16x16x32_f16 v[196:199], v[240:243], v[232:235], 0
	v_cvt_pk_f16_f32 v182, v136, v137
	v_cvt_pk_f16_f32 v183, v138, v139
	v_pk_max_f16 v182, v182, 0
	v_pk_max_f16 v183, v183, 0
	v_mfma_f32_16x16x32_f16 v[196:199], v[244:247], v[236:239], v[196:199]
	v_cvt_pk_f16_f32 v188, v184, v185
	v_cvt_pk_f16_f32 v189, v186, v187
	v_pk_max_f16 v188, v188, 0
	v_pk_max_f16 v189, v189, 0
	v_cvt_pk_f16_f32 v190, v160, v161
	v_cvt_pk_f16_f32 v191, v162, v163
	v_pk_max_f16 v190, v190, 0
	v_pk_max_f16 v191, v191, 0
	v_mfma_f32_16x16x32_f16 v[122:125], v[240:243], v[180:183], 0
	s_nop 0
	v_mfma_f32_16x16x32_f16 v[122:125], v[244:247], v[188:191], v[122:125]
	v_add_u32_e32 v145, 0x12c00, v105
	ds_read_b128 v[240:243], v145 offset:2048
	ds_read_b128 v[244:247], v145 offset:2064
	ds_read_b128 v[248:251], v145 offset:2080
	s_load_dword s30, s[12:13], 0x0
	v_cndmask_b32_e64 v0, v252, v192, s[2:3]
	ds_read_b128 v[252:255], v145 offset:2096
	v_cndmask_b32_e64 v0, v0, v196, s[0:1]
	v_cndmask_b32_e64 v0, v0, v122, s[26:27]
	ds_write_b32 v112, v0
	s_waitcnt vmcnt(16)
	v_cndmask_b32_e64 v1, v30, v134, s[0:1]
	v_bfi_b32 v30, s10, v1, v30
	v_perm_b32 v1, v22, v134, s24
	v_cndmask_b32_e64 v22, v22, v1, s[0:1]
	v_bfi_b32 v1, s10, v135, v18
	v_perm_b32 v121, v10, v135, s24
	v_cndmask_b32_e64 v18, v18, v1, s[0:1]
	v_cndmask_b32_e64 v10, v10, v121, s[0:1]
	s_add_i32 s22, s22, 0x80000
	s_add_i32 s11, s11, 1
	s_add_u32 s12, s12, 4
	s_addc_u32 s13, s13, 0
	v_add_u32_e32 v104, 0x400, v104
	v_add_u32_e32 v105, 0x800, v105
	v_add_u32_e32 v114, 2, v114
	s_cmp_eq_u32 s22, 0x898000
	s_waitcnt lgkmcnt(0)
	s_barrier
	ds_read_b128 v[232:235], v113
	ds_read_b128 v[236:239], v113 offset:1024
	s_waitcnt lgkmcnt(0)
	v_add_f32_e32 v0, v232, v233
	v_add_f32_e32 v1, v234, v235
	v_add_f32_e32 v121, v236, v237
	v_add_f32_e32 v144, v238, v239
	v_add_f32_e32 v0, v0, v1
	v_add_f32_e32 v121, v121, v144
	v_add_f32_e32 v0, v0, v121
	v_add_f32_e32 v0, s30, v0
	ds_write_b32 v106, v0
	v_cvt_f16_f32_e32 v1, v0
	v_cvt_f16_f32_e32 v121, v0
	s_nop 1
	v_permlane16_swap_b32_e32 v1, v121
	v_mov_b32_e32 v144, v1
	v_mov_b32_e32 v145, v121
	s_nop 1
	v_permlane32_swap_b32_e32 v1, v144
	v_permlane32_swap_b32_e32 v121, v145
	v_add_u32_e32 v106, 4, v106
	s_cbranch_scc0 .LBB1_4
